# E3 flag wait polls both unit flags in one round trip
# speedup vs baseline: 1.0025x; 1.0025x over previous
; __device__ __forceinline__ int lane_id() { int l; asm volatile("v_mbcnt_lo_u32_b32 %0, -1, 0\n\tv_mbcnt_hi_u32_b32 %0, -1, %0" : "=v"(l)); return l; }
; __device__ __forceinline__ unsigned xb_ld(unsigned* p)              { return __hip_atomic_load(p, __ATOMIC_RELAXED, __HIP_MEMORY_SCOPE_AGENT); }
; #define XB_SPIN(cond, bar) do { unsigned _sp = 0; while (cond) { __builtin_amdgcn_s_sleep(1); \
;     if ((++_sp & 255u) == 0u) { if (xb_ld(&(bar)[XB_TMO])) break; if (_sp > XB_SPIN_CAP) { atomicAdd(&(bar)[XB_TMO], 1u); break; } } } } while (0)
; __device__ __forceinline__ unsigned char* karg_ws() { return (unsigned char*)(GAS unsigned char*)karg_u64<15>(); }
; __device__ __forceinline__ void mflag_wait(int b, int m64, unsigned tag, int wave_s) {
;     if (wave_s == 0 && lane_id() == 0) {
;         unsigned* bar = (unsigned*)(karg_ws() + WS_CTL) + 4096; unsigned* f = (unsigned*)(karg_ws() + WS_CTL) + CTL_MFLAG + 16 * (128 * b + 2 * m64);
;         XB_SPIN(xb_ld(f) < tag || xb_ld(f + 16) < tag, bar);
;         __builtin_amdgcn_fence(__ATOMIC_ACQUIRE, "agent");
;         asm volatile("s_waitcnt vmcnt(0)" ::: "memory");
;     }
.LBB0_1662:
	global_load_dword v0, v1, s[22:23] sc1
	global_load_dword v207, v1, s[22:23] offset:64 sc1
	s_waitcnt vmcnt(0)
	v_min_u32_e32 v0, v0, v207
	v_cmp_ge_u32_e64 s[26:27], s96, v0

; __device__ __forceinline__ int lane_id() { int l; asm volatile("v_mbcnt_lo_u32_b32 %0, -1, 0\n\tv_mbcnt_hi_u32_b32 %0, -1, %0" : "=v"(l)); return l; }
; __device__ __forceinline__ unsigned xb_ld(unsigned* p)              { return __hip_atomic_load(p, __ATOMIC_RELAXED, __HIP_MEMORY_SCOPE_AGENT); }
; #define XB_SPIN(cond, bar) do { unsigned _sp = 0; while (cond) { __builtin_amdgcn_s_sleep(1); \
;     if ((++_sp & 255u) == 0u) { if (xb_ld(&(bar)[XB_TMO])) break; if (_sp > XB_SPIN_CAP) { atomicAdd(&(bar)[XB_TMO], 1u); break; } } } } while (0)
; __device__ __forceinline__ unsigned char* karg_ws() { return (unsigned char*)(GAS unsigned char*)karg_u64<15>(); }
; __device__ __forceinline__ void mflag_wait(int b, int m64, unsigned tag, int wave_s) {
;     if (wave_s == 0 && lane_id() == 0) {
;         unsigned* bar = (unsigned*)(karg_ws() + WS_CTL) + 4096; unsigned* f = (unsigned*)(karg_ws() + WS_CTL) + CTL_MFLAG + 16 * (128 * b + 2 * m64);
;         XB_SPIN(xb_ld(f) < tag || xb_ld(f + 16) < tag, bar);
;         __builtin_amdgcn_fence(__ATOMIC_ACQUIRE, "agent");
;         asm volatile("s_waitcnt vmcnt(0)" ::: "memory");
;     }
.LBB0_1728:
	global_load_dword v2, v1, s[28:29] sc1
	global_load_dword v207, v1, s[28:29] offset:64 sc1
	s_waitcnt vmcnt(0)
	v_min_u32_e32 v2, v2, v207
	v_cmp_ge_u32_e64 s[34:35], s96, v2
